# fp8 GEMM LDS fragment reads re-addressed (16B chunks fq, fq+4 instead of 2fq, 2fq+1): removes 2-way bank conflicts; same k permutation for A and B
# speedup vs baseline: 1.0173x; 1.0173x over previous
.LBB0_1766:
	v_lshrrev_b32_e32 v19, 4, v18
	v_and_b32_e32 v20, 15, v18
	s_lshl_b32 s1, s1, 5
	v_lshl_or_b32 v1, s10, 6, v20
	v_bfe_u32 v19, v19, 1, 1
	s_lshl_b32 s10, s10, 13
	s_and_b32 s1, s1, 0x60
	s_add_i32 m0, s47, 0x18000
	v_lshl_add_u64 v[10:11], v[10:11], 0, s[6:7]
	v_lshl_or_b32 v24, v19, 10, s10
	s_lshr_b32 s10, s1, 3
	s_waitcnt vmcnt(2)
	s_barrier
	global_load_lds_dwordx4 v[10:11], off
	v_lshl_add_u64 v[8:9], v[8:9], 0, s[6:7]
	s_add_i32 m0, s47, 0x1a000
	s_add_i32 s63, s47, 0x8000
	s_add_i32 s64, s47, 0xa000
	v_or_b32_e32 v19, s10, v19
	global_load_lds_dwordx4 v[8:9], off
	v_lshl_add_u64 v[4:5], v[4:5], 0, s[6:7]
	s_mov_b32 m0, s63
	s_add_u32 s10, s52, 0x40080
	global_load_lds_dwordx4 v[4:5], off
	v_lshl_add_u64 v[4:5], v[6:7], 0, s[6:7]
	s_mov_b32 m0, s64
	s_addc_u32 s11, s53, 0
	global_load_lds_dwordx4 v[4:5], off
	s_add_i32 m0, s47, 0x1c000
	v_lshl_add_u64 v[4:5], s[10:11], 0, v[2:3]
	global_load_lds_dwordx4 v[4:5], off
	v_lshl_add_u64 v[4:5], s[10:11], 0, v[164:165]
	s_add_i32 m0, s47, 0x1e000
	v_lshlrev_b32_e32 v22, 1, v18
	global_load_lds_dwordx4 v[4:5], off
	v_lshlrev_b32_e32 v4, 14, v16
	v_and_b32_e32 v4, 0xffff8000, v4
	v_lshl_add_u32 v4, v15, 11, v4
	v_and_b32_e32 v5, 1, v16
	v_lshl_or_b32 v4, v5, 6, v4
	v_bfe_u32 v21, v18, 4, 2
	v_and_b32_e32 v22, 32, v22
	v_lshlrev_b32_e32 v20, 6, v20
	v_lshlrev_b32_e32 v18, 2, v18
	v_lshl_add_u32 v170, v17, 1, v4
	v_lshlrev_b32_e32 v4, 14, v12
	v_or_b32_e32 v23, v20, v22
	v_and_b32_e32 v18, 32, v18
	v_and_b32_e32 v4, 0xffff8000, v4
	v_bitop3_b32 v20, v20, v18, v22 bitop3:0x36
	v_bitop3_b32 v25, v23, v18, 16 bitop3:0x36
	s_waitcnt vmcnt(6)
	v_lshl_add_u32 v4, v13, 11, v4
	v_and_b32_e32 v5, 1, v12
	v_or_b32_e32 v20, v20, v24
	v_or_b32_e32 v22, 16, v23
	v_or_b32_e32 v24, v25, v24
	v_lshlrev_b32_e32 v19, 10, v19
	s_cmpk_lt_u32 s0, 0x100
	v_lshl_or_b32 v4, v5, 6, v4
	v_bitop3_b32 v190, v19, v23, v18 bitop3:0xf6
	v_bitop3_b32 v191, v22, v19, v18 bitop3:0xde
	s_cselect_b64 s[14:15], -1, 0
	v_lshl_or_b32 v192, v21, 3, s1
	v_mov_b32_e32 v171, v3
	v_lshl_add_u32 v172, v14, 1, v4
	v_mov_b32_e32 v173, v3
	s_mov_b32 s65, 0
	v_add_u32_e32 v193, 0, v20
	v_add_u32_e32 v194, 0, v24
	v_and_b32_e32 v193, 15, v0
	v_lshlrev_b32_e32 v193, 6, v193
	v_bfe_u32 v194, v0, 4, 2
	v_lshl_or_b32 v193, v194, 4, v193
	v_and_b32_e32 v194, 8, v0
	v_lshlrev_b32_e32 v194, 2, v194
	v_xor_b32_e32 v193, v193, v194
	v_bfe_u32 v190, v0, 6, 2
	v_lshl_or_b32 v190, v190, 12, v193
	v_or_b32_e32 v191, 0x400, v190
	v_lshrrev_b32_e32 v194, 8, v0
	v_lshl_or_b32 v193, v194, 13, v193
	v_or_b32_e32 v194, 0x400, v193
	s_barrier
	s_branch .LBB0_1769

.LBB0_1802:
	v_lshrrev_b32_e32 v19, 4, v18
	v_and_b32_e32 v20, 15, v18
	v_lshl_or_b32 v1, s0, 6, v20
	v_bfe_u32 v19, v19, 1, 1
	s_lshl_b32 s0, s0, 13
	v_lshl_or_b32 v24, v19, 10, s0
	s_lshl_b32 s0, s1, 5
	s_and_b32 s11, s0, 0x60
	s_add_i32 m0, s49, 0x18000
	v_lshl_add_u64 v[10:11], v[10:11], 0, s[6:7]
	s_lshr_b32 s0, s11, 3
	s_waitcnt vmcnt(2)
	s_barrier
	global_load_lds_dwordx4 v[10:11], off
	v_lshl_add_u64 v[8:9], v[8:9], 0, s[6:7]
	s_add_i32 m0, s49, 0x1a000
	s_add_i32 s74, s49, 0x8000
	s_add_i32 s75, s49, 0xa000
	v_or_b32_e32 v19, s0, v19
	global_load_lds_dwordx4 v[8:9], off
	v_lshl_add_u64 v[4:5], v[4:5], 0, s[6:7]
	s_mov_b32 m0, s74
	s_add_u32 s0, s54, 0x40080
	global_load_lds_dwordx4 v[4:5], off
	v_lshl_add_u64 v[4:5], v[6:7], 0, s[6:7]
	s_mov_b32 m0, s75
	s_addc_u32 s1, s55, 0
	global_load_lds_dwordx4 v[4:5], off
	s_add_i32 m0, s49, 0x1c000
	v_lshl_add_u64 v[4:5], s[0:1], 0, v[2:3]
	global_load_lds_dwordx4 v[4:5], off
	v_lshl_add_u64 v[4:5], s[0:1], 0, v[168:169]
	s_add_i32 m0, s49, 0x1e000
	v_lshlrev_b32_e32 v22, 1, v18
	global_load_lds_dwordx4 v[4:5], off
	v_lshlrev_b32_e32 v4, 14, v12
	v_and_b32_e32 v4, 0xffff8000, v4
	v_lshl_add_u32 v4, v13, 11, v4
	v_and_b32_e32 v5, 1, v12
	v_lshl_or_b32 v4, v5, 6, v4
	v_bfe_u32 v21, v18, 4, 2
	v_and_b32_e32 v22, 32, v22
	v_lshlrev_b32_e32 v20, 6, v20
	v_lshlrev_b32_e32 v18, 2, v18
	v_lshl_add_u32 v170, v14, 1, v4
	v_lshlrev_b32_e32 v4, 14, v15
	v_or_b32_e32 v23, v20, v22
	v_and_b32_e32 v18, 32, v18
	v_and_b32_e32 v4, 0xffff8000, v4
	v_bitop3_b32 v20, v20, v18, v22 bitop3:0x36
	v_bitop3_b32 v25, v23, v18, 16 bitop3:0x36
	s_waitcnt vmcnt(6)
	v_lshl_add_u32 v4, v16, 11, v4
	v_and_b32_e32 v5, 1, v15
	v_or_b32_e32 v20, v20, v24
	v_or_b32_e32 v22, 16, v23
	v_or_b32_e32 v24, v25, v24
	v_lshlrev_b32_e32 v19, 10, v19
	s_cmpk_lt_u32 s10, 0x100
	v_lshl_or_b32 v4, v5, 6, v4
	v_bitop3_b32 v190, v19, v23, v18 bitop3:0xf6
	v_bitop3_b32 v191, v22, v19, v18 bitop3:0xde
	s_cselect_b64 s[36:37], -1, 0
	v_lshl_or_b32 v192, v21, 3, s11
	v_mov_b32_e32 v171, v3
	v_lshl_add_u32 v172, v17, 1, v4
	v_mov_b32_e32 v173, v3
	s_mov_b32 s76, 0
	v_add_u32_e32 v193, 0, v20
	v_add_u32_e32 v194, 0, v24
	v_and_b32_e32 v193, 15, v0
	v_lshlrev_b32_e32 v193, 6, v193
	v_bfe_u32 v194, v0, 4, 2
	v_lshl_or_b32 v193, v194, 4, v193
	v_and_b32_e32 v194, 8, v0
	v_lshlrev_b32_e32 v194, 2, v194
	v_xor_b32_e32 v193, v193, v194
	v_bfe_u32 v190, v0, 6, 2
	v_lshl_or_b32 v190, v190, 12, v193
	v_or_b32_e32 v191, 0x400, v190
	v_lshrrev_b32_e32 v194, 8, v0
	v_lshl_or_b32 v193, v194, 13, v193
	v_or_b32_e32 v194, 0x400, v193
	s_barrier
	s_branch .LBB0_1805

.LBB0_1880:
	v_readlane_b32 s40, v254, 24
	v_lshrrev_b32_e32 v15, 4, v14
	v_and_b32_e32 v20, 15, v14
	s_lshl_b32 s1, s1, 5
	v_mov_b32_e32 v169, v3
	v_readlane_b32 s41, v254, 25
	v_lshl_or_b32 v1, s4, 6, v20
	v_bfe_u32 v15, v15, 1, 1
	s_lshl_b32 s4, s4, 13
	s_and_b32 s1, s1, 0x60
	s_add_i32 m0, s11, 0x18000
	v_lshl_add_u64 v[4:5], v[4:5], 0, s[6:7]
	v_lshl_add_u64 v[16:17], s[40:41], 0, v[168:169]
	v_mov_b32_e32 v167, v3
	v_lshl_or_b32 v24, v15, 10, s4
	s_lshr_b32 s4, s1, 3
	s_waitcnt vmcnt(2)
	s_barrier
	global_load_lds_dwordx4 v[4:5], off
	v_lshl_add_u64 v[4:5], v[6:7], 0, s[6:7]
	s_add_i32 m0, s11, 0x1a000
	s_add_i32 s52, s11, 0x8000
	s_add_i32 s53, s11, 0xa000
	v_lshl_add_u64 v[18:19], s[40:41], 0, v[166:167]
	v_or_b32_e32 v15, s4, v15
	global_load_lds_dwordx4 v[4:5], off
	v_lshl_add_u64 v[4:5], v[16:17], 0, s[6:7]
	s_mov_b32 m0, s52
	s_add_u32 s4, s44, 0xb0080
	global_load_lds_dwordx4 v[4:5], off
	v_lshl_add_u64 v[4:5], v[18:19], 0, s[6:7]
	s_mov_b32 m0, s53
	s_addc_u32 s5, s45, 0
	global_load_lds_dwordx4 v[4:5], off
	s_add_i32 m0, s11, 0x1c000
	v_lshl_add_u64 v[4:5], s[4:5], 0, v[2:3]
	global_load_lds_dwordx4 v[4:5], off
	v_lshl_add_u64 v[4:5], s[4:5], 0, v[164:165]
	s_add_i32 m0, s11, 0x1e000
	s_movk_i32 s5, 0x1600
	global_load_lds_dwordx4 v[4:5], off
	v_bfe_u32 v21, v14, 4, 2
	v_lshrrev_b32_e32 v5, 1, v12
	v_mul_lo_u32 v4, v11, s5
	s_mov_b32 s4, 0x16000
	s_cmpk_lt_u32 s0, 0x100
	v_lshl_or_b32 v192, v21, 3, s1
	v_mad_u64_u32 v[4:5], s[0:1], v5, s4, v[4:5]
	v_and_b32_e32 v5, 1, v12
	v_lshlrev_b32_e32 v22, 1, v14
	v_lshl_or_b32 v4, v5, 6, v4
	v_and_b32_e32 v22, 32, v22
	v_lshlrev_b32_e32 v20, 6, v20
	v_lshlrev_b32_e32 v14, 2, v14
	v_lshl_add_u32 v170, v13, 1, v4
	v_lshrrev_b32_e32 v5, 1, v8
	v_mul_lo_u32 v4, v9, s5
	v_or_b32_e32 v23, v20, v22
	v_and_b32_e32 v14, 32, v14
	v_mad_u64_u32 v[4:5], s[0:1], v5, s4, v[4:5]
	v_bitop3_b32 v20, v20, v14, v22 bitop3:0x36
	v_bitop3_b32 v25, v23, v14, 16 bitop3:0x36
	s_waitcnt vmcnt(6)
	v_and_b32_e32 v5, 1, v8
	v_or_b32_e32 v20, v20, v24
	v_or_b32_e32 v22, 16, v23
	v_or_b32_e32 v24, v25, v24
	v_lshlrev_b32_e32 v15, 10, v15
	v_lshl_or_b32 v4, v5, 6, v4
	v_readlane_b32 s0, v254, 20
	v_bitop3_b32 v190, v15, v23, v14 bitop3:0xf6
	v_bitop3_b32 v191, v22, v15, v14 bitop3:0xde
	s_cselect_b64 s[36:37], -1, 0
	v_mov_b32_e32 v171, v3
	v_lshl_add_u32 v172, v10, 1, v4
	v_mov_b32_e32 v173, v3
	s_mov_b32 s54, 0
	v_add_u32_e32 v193, 0, v20
	v_add_u32_e32 v194, 0, v24
	v_and_b32_e32 v193, 15, v0
	v_lshlrev_b32_e32 v193, 6, v193
	v_bfe_u32 v194, v0, 4, 2
	v_lshl_or_b32 v193, v194, 4, v193
	v_and_b32_e32 v194, 8, v0
	v_lshlrev_b32_e32 v194, 2, v194
	v_xor_b32_e32 v193, v193, v194
	v_bfe_u32 v190, v0, 6, 2
	v_lshl_or_b32 v190, v190, 12, v193
	v_or_b32_e32 v191, 0x400, v190
	v_lshrrev_b32_e32 v194, 8, v0
	v_lshl_or_b32 v193, v194, 13, v193
	v_or_b32_e32 v194, 0x400, v193
	v_readlane_b32 s57, v254, 9
	s_mov_b32 s58, s0
	s_barrier
	v_readlane_b32 s1, v254, 21
	s_branch .LBB0_1883

.LBB0_1904:
	v_lshrrev_b32_e32 v5, 4, v4
	v_and_b32_e32 v14, 15, v4
	s_lshl_b32 s1, s1, 5
	v_lshl_or_b32 v1, s10, 6, v14
	v_lshlrev_b32_e32 v16, 1, v4
	v_bfe_u32 v5, v5, 1, 1
	s_lshl_b32 s10, s10, 13
	s_and_b32 s1, s1, 0x60
	v_bfe_u32 v15, v4, 4, 2
	v_and_b32_e32 v16, 32, v16
	v_lshlrev_b32_e32 v14, 6, v14
	v_lshl_or_b32 v18, v5, 10, s10
	v_lshlrev_b32_e32 v4, 2, v4
	s_lshr_b32 s10, s1, 3
	v_or_b32_e32 v17, v14, v16
	v_and_b32_e32 v4, 32, v4
	v_or_b32_e32 v5, s10, v5
	v_lshl_add_u64 v[6:7], s[46:47], 0, v[2:3]
	v_mov_b32_e32 v141, v3
	v_readlane_b32 s48, v253, 58
	v_bitop3_b32 v14, v14, v4, v16 bitop3:0x36
	v_or_b32_e32 v16, 16, v17
	v_lshlrev_b32_e32 v5, 10, v5
	s_add_u32 s10, s46, 0xb0080
	v_lshl_add_u64 v[8:9], s[46:47], 0, v[140:141]
	v_mov_b32_e32 v145, v3
	v_readlane_b32 s49, v253, 59
	v_bitop3_b32 v19, v17, v4, 16 bitop3:0x36
	v_bitop3_b32 v154, v5, v17, v4 bitop3:0xf6
	v_bitop3_b32 v155, v16, v5, v4 bitop3:0xde
	s_addc_u32 s11, s47, 0
	s_add_i32 m0, s53, 0x18000
	v_lshl_add_u64 v[4:5], v[6:7], 0, s[6:7]
	v_lshl_add_u64 v[10:11], s[48:49], 0, v[144:145]
	v_mov_b32_e32 v143, v3
	s_waitcnt vmcnt(2)
	s_barrier
	global_load_lds_dwordx4 v[4:5], off
	v_lshl_add_u64 v[4:5], v[8:9], 0, s[6:7]
	s_add_i32 m0, s53, 0x1a000
	s_add_i32 s57, s53, 0x8000
	v_lshl_add_u64 v[12:13], s[48:49], 0, v[142:143]
	global_load_lds_dwordx4 v[4:5], off
	v_lshl_add_u64 v[4:5], v[10:11], 0, s[6:7]
	s_mov_b32 m0, s57
	s_add_i32 s58, s53, 0xa000
	global_load_lds_dwordx4 v[4:5], off
	v_lshl_add_u64 v[4:5], v[12:13], 0, s[6:7]
	s_mov_b32 m0, s58
	v_or_b32_e32 v14, v14, v18
	global_load_lds_dwordx4 v[4:5], off
	s_add_i32 m0, s53, 0x1c000
	v_lshl_add_u64 v[4:5], s[10:11], 0, v[2:3]
	global_load_lds_dwordx4 v[4:5], off
	v_lshl_add_u64 v[4:5], s[10:11], 0, v[140:141]
	s_add_i32 m0, s53, 0x1e000
	v_or_b32_e32 v18, v19, v18
	global_load_lds_dwordx4 v[4:5], off
	s_waitcnt vmcnt(6)
	s_cmpk_lt_u32 s0, 0x100
	v_readlane_b32 s0, v253, 26
	s_cselect_b64 s[36:37], -1, 0
	v_lshl_or_b32 v156, v15, 3, s1
	v_add_u32_e32 v157, 0, v14
	v_add_u32_e32 v158, 0, v18
	v_and_b32_e32 v157, 15, v0
	v_lshlrev_b32_e32 v157, 6, v157
	v_bfe_u32 v158, v0, 4, 2
	v_lshl_or_b32 v157, v158, 4, v157
	v_and_b32_e32 v158, 8, v0
	v_lshlrev_b32_e32 v158, 2, v158
	v_xor_b32_e32 v157, v157, v158
	v_bfe_u32 v154, v0, 6, 2
	v_lshl_or_b32 v154, v154, 12, v157
	v_or_b32_e32 v155, 0x400, v154
	v_lshrrev_b32_e32 v158, 8, v0
	v_lshl_or_b32 v157, v158, 13, v157
	v_or_b32_e32 v158, 0x400, v157
	v_readlane_b32 s59, v251, 38
	s_mov_b32 s44, s0
	v_readlane_b32 s45, v254, 3
	v_readlane_b32 s64, v253, 53
	s_barrier
	s_branch .LBB0_1907

.LBB0_1938:
	v_lshrrev_b32_e32 v19, 4, v18
	v_and_b32_e32 v20, 15, v18
	s_lshl_b32 s1, s1, 5
	v_lshl_or_b32 v1, s4, 6, v20
	v_bfe_u32 v19, v19, 1, 1
	s_lshl_b32 s4, s4, 13
	s_and_b32 s1, s1, 0x60
	s_add_i32 m0, s59, 0x18000
	v_lshl_add_u64 v[10:11], v[10:11], 0, s[6:7]
	v_lshl_or_b32 v24, v19, 10, s4
	s_lshr_b32 s4, s1, 3
	s_waitcnt vmcnt(2)
	s_barrier
	global_load_lds_dwordx4 v[10:11], off
	v_lshl_add_u64 v[8:9], v[8:9], 0, s[6:7]
	s_add_i32 m0, s59, 0x1a000
	s_add_i32 s64, s59, 0x8000
	s_add_i32 s65, s59, 0xa000
	v_or_b32_e32 v19, s4, v19
	global_load_lds_dwordx4 v[8:9], off
	v_lshl_add_u64 v[4:5], v[4:5], 0, s[6:7]
	s_mov_b32 m0, s64
	s_add_u32 s4, s46, 0x58080
	global_load_lds_dwordx4 v[4:5], off
	v_lshl_add_u64 v[4:5], v[6:7], 0, s[6:7]
	s_mov_b32 m0, s65
	s_addc_u32 s5, s47, 0
	global_load_lds_dwordx4 v[4:5], off
	s_add_i32 m0, s59, 0x1c000
	v_lshl_add_u64 v[4:5], s[4:5], 0, v[2:3]
	global_load_lds_dwordx4 v[4:5], off
	v_lshl_add_u64 v[4:5], s[4:5], 0, v[164:165]
	s_add_i32 m0, s59, 0x1e000
	s_movk_i32 s4, 0xb00
	global_load_lds_dwordx4 v[4:5], off
	v_bfe_u32 v21, v18, 4, 2
	v_lshrrev_b32_e32 v5, 1, v16
	v_mul_lo_u32 v4, v15, s4
	s_mov_b32 s5, 0xb000
	s_cmpk_lt_u32 s0, 0x100
	v_lshl_or_b32 v192, v21, 3, s1
	v_mad_u64_u32 v[4:5], s[0:1], v5, s5, v[4:5]
	v_and_b32_e32 v5, 1, v16
	v_lshlrev_b32_e32 v22, 1, v18
	v_lshl_or_b32 v4, v5, 6, v4
	v_and_b32_e32 v22, 32, v22
	v_lshlrev_b32_e32 v20, 6, v20
	v_lshlrev_b32_e32 v18, 2, v18
	v_lshl_add_u32 v170, v17, 1, v4
	v_lshrrev_b32_e32 v5, 1, v12
	v_mul_lo_u32 v4, v13, s4
	v_or_b32_e32 v23, v20, v22
	v_and_b32_e32 v18, 32, v18
	v_mad_u64_u32 v[4:5], s[0:1], v5, s5, v[4:5]
	v_bitop3_b32 v20, v20, v18, v22 bitop3:0x36
	v_bitop3_b32 v25, v23, v18, 16 bitop3:0x36
	s_waitcnt vmcnt(6)
	v_and_b32_e32 v5, 1, v12
	v_or_b32_e32 v20, v20, v24
	v_or_b32_e32 v22, 16, v23
	v_or_b32_e32 v24, v25, v24
	v_lshlrev_b32_e32 v19, 10, v19
	v_lshl_or_b32 v4, v5, 6, v4
	v_bitop3_b32 v190, v19, v23, v18 bitop3:0xf6
	v_bitop3_b32 v191, v22, v19, v18 bitop3:0xde
	s_cselect_b64 s[38:39], -1, 0
	s_ashr_i32 s15, s14, 31
	v_mov_b32_e32 v171, v3
	v_lshl_add_u32 v172, v14, 1, v4
	v_mov_b32_e32 v173, v3
	s_mov_b32 s67, 0
	v_add_u32_e32 v193, 0, v20
	v_add_u32_e32 v194, 0, v24
	v_and_b32_e32 v193, 15, v0
	v_lshlrev_b32_e32 v193, 6, v193
	v_bfe_u32 v194, v0, 4, 2
	v_lshl_or_b32 v193, v194, 4, v193
	v_and_b32_e32 v194, 8, v0
	v_lshlrev_b32_e32 v194, 2, v194
	v_xor_b32_e32 v193, v193, v194
	v_bfe_u32 v190, v0, 6, 2
	v_lshl_or_b32 v190, v190, 12, v193
	v_or_b32_e32 v191, 0x400, v190
	v_lshrrev_b32_e32 v194, 8, v0
	v_lshl_or_b32 v193, v194, 13, v193
	v_or_b32_e32 v194, 0x400, v193
	s_mov_b64 s[24:25], s[48:49]
	s_barrier
	s_branch .LBB0_1941
